# speedup vs baseline: 1.0237x; 1.0201x over previous
_Z7k0_prepPKfS0_S0_S0_S0_S0_S0_S0_S0_S0_S0_S0_S0_Pf:
	s_movk_i32 s3, 0xffb0
	s_cmp_lt_u32 s2, 80
	s_cselect_b32 s3, 0x19c, s3
	s_add_i32 s2, s2, s3
	s_load_dwordx2 s[8:9], s[0:1], 0x68
	s_cmpk_gt_i32 s2, 0x17f
	s_mov_b64 s[4:5], -1
	s_cbranch_scc0 .LBB0_71
	s_cmpk_lt_u32 s2, 0x19f
	s_cbranch_scc0 .LBB0_42
	s_load_dwordx2 s[4:5], s[0:1], 0x30
	s_cmpk_lg_i32 s2, 0x19e
	s_mov_b64 s[6:7], -1
	s_cbranch_scc0 .LBB0_34
	s_load_dwordx2 s[6:7], s[0:1], 0x20
	v_lshl_or_b32 v1, s2, 8, v0
	v_add_u32_e32 v2, 0xfffe8000, v1
	s_movk_i32 s3, 0x1a00
	v_cmp_gt_u32_e32 vcc, s3, v2
	s_and_saveexec_b64 s[10:11], vcc
	s_xor_b64 s[10:11], exec, s[10:11]
	s_cbranch_execz .LBB0_29
	v_lshrrev_b32_e32 v3, 6, v2
	s_movk_i32 s3, 0x1ff
	v_add_u32_e32 v4, 4, v3
	v_cmp_lt_u32_e32 vcc, s3, v2
	v_and_b32_e32 v1, 63, v0
	v_and_b32_e32 v7, 15, v0
	v_cndmask_b32_e32 v5, v3, v4, vcc
	v_subrev_u32_e32 v2, 36, v5
	v_bfe_u32 v6, v0, 4, 2
	v_cmp_lt_u32_e32 vcc, 7, v2
	s_and_saveexec_b64 s[12:13], vcc
	s_xor_b64 s[12:13], exec, s[12:13]
	s_cbranch_execz .LBB0_26
	v_cmp_lt_u32_e32 vcc, 7, v5
	s_and_saveexec_b64 s[14:15], vcc
	s_xor_b64 s[14:15], exec, s[14:15]
	s_cbranch_execz .LBB0_23
	v_cmp_lt_u32_e32 vcc, 19, v5
	s_and_saveexec_b64 s[16:17], vcc
	s_xor_b64 s[16:17], exec, s[16:17]
	s_cbranch_execz .LBB0_20
	v_cmp_lt_u32_e32 vcc, 27, v5
	s_and_saveexec_b64 s[18:19], vcc
	s_xor_b64 s[18:19], exec, s[18:19]
	s_cbranch_execz .LBB0_17
	v_cmp_lt_u32_e32 vcc, 35, v5
	s_and_saveexec_b64 s[20:21], vcc
	s_xor_b64 s[20:21], exec, s[20:21]
	s_cbranch_execz .LBB0_14
	s_load_dwordx2 s[22:23], s[0:1], 0x60
	s_movk_i32 s3, 0x4b
	v_cmp_lt_u32_e32 vcc, s3, v5
	s_and_saveexec_b64 s[24:25], vcc
	s_xor_b64 s[24:25], exec, s[24:25]
	v_add_u32_e32 v2, 0xffffffb4, v5
	v_lshrrev_b32_e32 v9, 3, v2
	v_and_b32_e32 v8, 7, v2
	s_or_saveexec_b64 s[24:25], s[24:25]
	v_mov_b32_e32 v10, 0x100
	s_waitcnt lgkmcnt(0)
	v_mov_b64_e32 v[2:3], s[22:23]
	s_xor_b64 exec, exec, s[24:25]
	s_cbranch_execz .LBB0_13
	s_load_dwordx2 s[22:23], s[0:1], 0x58
	v_subrev_u32_e32 v2, 44, v5
	v_ashrrev_i32_e32 v9, 1, v2
	v_and_b32_e32 v8, 1, v5
	v_mov_b32_e32 v10, 64
	s_waitcnt lgkmcnt(0)
	v_mov_b64_e32 v[2:3], s[22:23]

.LBB0_50:
	s_or_b64 exec, exec, s[6:7]
	s_waitcnt vmcnt(7)
	v_mul_f32_e32 v7, 0.5, v4
	v_max_f32_e32 v14, v20, v20
	v_max_f32_e32 v7, v14, v7
	s_waitcnt vmcnt(6)
	v_mul_f32_e32 v14, 0.5, v1
	v_max_f32_e32 v15, v26, v26
	v_max_f32_e32 v14, v15, v14
	v_mul_f32_e32 v1, 0x3fc00000, v1
	v_min_f32_e32 v1, v14, v1
	v_max_f32_e32 v14, 0, v1
	s_waitcnt vmcnt(5)
	v_mul_f32_e32 v1, 0.5, v2
	v_max_f32_e32 v15, v25, v25
	v_mul_f32_e32 v4, 0x3fc00000, v4
	v_max_f32_e32 v1, v15, v1
	v_mul_f32_e32 v2, 0x3fc00000, v2
	v_min_f32_e32 v4, v7, v4
	v_min_f32_e32 v1, v1, v2
	v_max_f32_e32 v4, 0, v4
	v_max_f32_e32 v15, 0, v1
	s_waitcnt vmcnt(3)
	v_fma_f32 v7, v28, v4, 0
	s_waitcnt vmcnt(1)
	v_pk_mul_f32 v[18:19], v[10:11], v[14:15]
	v_mul_f32_e32 v2, 0.5, v3
	v_add_f32_e32 v1, v7, v18
	v_max_f32_e32 v7, v24, v24
	v_max_f32_e32 v2, v7, v2
	v_mul_f32_e32 v3, 0x3fc00000, v3
	v_min_f32_e32 v2, v2, v3
	v_mul_f32_e32 v3, 0.5, v6
	s_waitcnt vmcnt(0)
	v_max_f32_e32 v7, v5, v5
	v_max_f32_e32 v3, v7, v3
	v_mul_f32_e32 v6, 0x3fc00000, v6
	v_min_f32_e32 v3, v3, v6
	v_max_f32_e32 v2, 0, v2
	v_max_f32_e32 v3, 0, v3
	v_pk_mul_f32 v[6:7], v[8:9], v[2:3]
	v_add_f32_e32 v1, v1, v19
	v_add_f32_e32 v1, v1, v6
	v_add_f32_e32 v1, v1, v7
	s_mov_b64 s[6:7], 0xc100
	v_lshl_add_u64 v[16:17], v[12:13], 2, s[8:9]
	v_mul_f32_e32 v29, v28, v4
	v_lshlrev_b64 v[30:31], v22, -1
	v_add_f32_dpp v1, v1, v1 quad_perm:[1,0,3,2] row_mask:0xf bank_mask:0xf bound_ctrl:1
	v_not_b32_e32 v27, v30
	v_not_b32_e32 v4, v31
	v_add_f32_dpp v1, v1, v1 quad_perm:[2,3,0,1] row_mask:0xf bank_mask:0xf bound_ctrl:1
	v_mov_b32_e32 v3, v13
	s_nop 0
	v_add_f32_dpp v1, v1, v1 row_half_mirror row_mask:0xf bank_mask:0xf bound_ctrl:1
	s_nop 1
	v_add_f32_dpp v1, v1, v1 row_mirror row_mask:0xf bank_mask:0xf bound_ctrl:1
	s_nop 0
	v_readlane_b32 s26, v1, 0
	v_readlane_b32 s27, v1, 16
	v_readlane_b32 s28, v1, 32
	v_readlane_b32 s29, v1, 48
	s_nop 1
	v_mov_b32_e32 v14, s27
	v_mov_b32_e32 v2, s29
	v_add_f32_e32 v14, s26, v14
	v_add_f32_e32 v2, s28, v2
	v_add_f32_e32 v1, v14, v2
	v_mov_b32_e32 v2, 0x358637bd
	v_cmp_neq_f32_e32 vcc, 0, v1
	s_nop 1
	v_cndmask_b32_e32 v1, v2, v1, vcc
	v_lshlrev_b32_e32 v2, 4, v21
	v_lshl_add_u64 v[2:3], v[2:3], 2, s[8:9]
	v_lshl_add_u64 v[2:3], v[2:3], 0, s[6:7]
	s_mov_b64 s[6:7], 0x10dc0
	v_lshl_add_u64 v[12:13], v[16:17], 0, s[6:7]
	s_mov_b64 s[6:7], 0x6ce64
	v_lshl_add_u64 v[14:15], v[16:17], 0, s[6:7]
	s_mov_b64 s[6:7], 0xc8f08
	v_lshl_add_u64 v[16:17], v[16:17], 0, s[6:7]
	v_div_scale_f32 v21, s[6:7], v1, v1, v29
	v_rcp_f32_e32 v32, v21
	s_nop 0
	v_fma_f32 v30, -v21, v32, 1.0
	v_fmac_f32_e32 v32, v30, v32
	v_div_scale_f32 v30, vcc, v29, v1, v29
	v_mul_f32_e32 v31, v30, v32
	v_fma_f32 v33, -v21, v31, v30
	v_fmac_f32_e32 v31, v33, v32
	v_fma_f32 v21, -v21, v31, v30
	v_div_fmas_f32 v21, v21, v32, v31
	v_div_fixup_f32 v21, v21, v1, v29
	v_sub_f32_e32 v21, v21, v20
	v_add_f32_e32 v29, v20, v21
	v_cmp_neq_f32_e32 vcc, 0, v28
	v_cmp_neq_f32_e64 s[6:7], 0, v29
	s_or_b64 s[6:7], vcc, s[6:7]
	s_nop 0
	v_cndmask_b32_e64 v20, 0, 1, s[6:7]
	v_cmp_ne_u32_e32 vcc, 0, v20
	s_and_saveexec_b64 s[12:13], s[6:7]
	s_cbranch_execz .LBB0_53
	v_and_b32_e32 v21, vcc_lo, v27
	v_and_b32_e32 v20, vcc_hi, v4
	v_bcnt_u32_b32 v21, v21, 0
	v_bcnt_u32_b32 v20, v20, v21
	v_mov_b32_e32 v21, 0
	v_lshlrev_b32_e32 v30, 2, v20
	v_mov_b32_e32 v31, v21
	v_lshl_add_u64 v[32:33], v[12:13], 0, v[30:31]
	global_store_dword v[32:33], v22, off
	v_lshl_add_u64 v[32:33], v[14:15], 0, v[30:31]
	v_lshl_add_u64 v[30:31], v[16:17], 0, v[30:31]
	v_cmp_gt_u64_e64 s[6:7], 3, v[20:21]
	global_store_dword v[32:33], v28, off
	global_store_dword v[30:31], v29, off
	s_and_b64 exec, exec, s[6:7]
	s_cbranch_execz .LBB0_53
	v_lshlrev_b32_e32 v20, 2, v20
	v_lshl_add_u64 v[20:21], v[2:3], 0, v[20:21]
	global_store_dword v[20:21], v22, off offset:4
	global_store_dword v[20:21], v28, off offset:16
	global_store_dword v[20:21], v29, off offset:28

	.amdhsa_kernel _Z7k0_prepPKfS0_S0_S0_S0_S0_S0_S0_S0_S0_S0_S0_S0_Pf
		.amdhsa_group_segment_fixed_size 1024
		.amdhsa_private_segment_fixed_size 0
		.amdhsa_kernarg_size 112
		.amdhsa_user_sgpr_count 2
		.amdhsa_user_sgpr_dispatch_ptr 0
		.amdhsa_user_sgpr_queue_ptr 0
		.amdhsa_user_sgpr_kernarg_segment_ptr 1
		.amdhsa_user_sgpr_dispatch_id 0
		.amdhsa_user_sgpr_kernarg_preload_length 0
		.amdhsa_user_sgpr_kernarg_preload_offset 0
		.amdhsa_user_sgpr_private_segment_size 0
		.amdhsa_uses_dynamic_stack 0
		.amdhsa_enable_private_segment 0
		.amdhsa_system_sgpr_workgroup_id_x 1
		.amdhsa_system_sgpr_workgroup_id_y 0
		.amdhsa_system_sgpr_workgroup_id_z 0
		.amdhsa_system_sgpr_workgroup_info 0
		.amdhsa_system_vgpr_workitem_id 0
		.amdhsa_next_free_vgpr 58
		.amdhsa_next_free_sgpr 30
		.amdhsa_accum_offset 60
		.amdhsa_reserve_vcc 1
		.amdhsa_float_round_mode_32 0
		.amdhsa_float_round_mode_16_64 0
		.amdhsa_float_denorm_mode_32 3
		.amdhsa_float_denorm_mode_16_64 3
		.amdhsa_dx10_clamp 1
		.amdhsa_ieee_mode 1
		.amdhsa_fp16_overflow 0
		.amdhsa_tg_split 0
		.amdhsa_exception_fp_ieee_invalid_op 0
		.amdhsa_exception_fp_denorm_src 0
		.amdhsa_exception_fp_ieee_div_zero 0
		.amdhsa_exception_fp_ieee_overflow 0
		.amdhsa_exception_fp_ieee_underflow 0
		.amdhsa_exception_fp_ieee_inexact 0
		.amdhsa_exception_int_div_zero 0
	.end_amdhsa_kernel

amdhsa.kernels:
  - .agpr_count:     0
    .args:
      - .actual_access:  read_only
        .address_space:  global
        .offset:         0
        .size:           8
        .value_kind:     global_buffer
      - .actual_access:  read_only
        .address_space:  global
        .offset:         8
        .size:           8
        .value_kind:     global_buffer
      - .actual_access:  read_only
        .address_space:  global
        .offset:         16
        .size:           8
        .value_kind:     global_buffer
      - .actual_access:  read_only
        .address_space:  global
        .offset:         24
        .size:           8
        .value_kind:     global_buffer
      - .actual_access:  read_only
        .address_space:  global
        .offset:         32
        .size:           8
        .value_kind:     global_buffer
      - .actual_access:  read_only
        .address_space:  global
        .offset:         40
        .size:           8
        .value_kind:     global_buffer
      - .actual_access:  read_only
        .address_space:  global
        .offset:         48
        .size:           8
        .value_kind:     global_buffer
      - .actual_access:  read_only
        .address_space:  global
        .offset:         56
        .size:           8
        .value_kind:     global_buffer
      - .actual_access:  read_only
        .address_space:  global
        .offset:         64
        .size:           8
        .value_kind:     global_buffer
      - .actual_access:  read_only
        .address_space:  global
        .offset:         72
        .size:           8
        .value_kind:     global_buffer
      - .actual_access:  read_only
        .address_space:  global
        .offset:         80
        .size:           8
        .value_kind:     global_buffer
      - .actual_access:  read_only
        .address_space:  global
        .offset:         88
        .size:           8
        .value_kind:     global_buffer
      - .actual_access:  read_only
        .address_space:  global
        .offset:         96
        .size:           8
        .value_kind:     global_buffer
      - .actual_access:  write_only
        .address_space:  global
        .offset:         104
        .size:           8
        .value_kind:     global_buffer
    .group_segment_fixed_size: 1024
    .kernarg_segment_align: 8
    .kernarg_segment_size: 112
    .language:       OpenCL C
    .language_version:
      - 2
      - 0
    .max_flat_workgroup_size: 256
    .name:           _Z7k0_prepPKfS0_S0_S0_S0_S0_S0_S0_S0_S0_S0_S0_S0_Pf
    .private_segment_fixed_size: 0
    .sgpr_count:     36
    .sgpr_spill_count: 0
    .symbol:         _Z7k0_prepPKfS0_S0_S0_S0_S0_S0_S0_S0_S0_S0_S0_S0_Pf.kd
    .uniform_work_group_size: 1
    .uses_dynamic_stack: false
    .vgpr_count:     58
    .vgpr_spill_count: 0
    .wavefront_size: 64
  - .agpr_count:     0
    .args:
      - .actual_access:  read_only
        .address_space:  global
        .offset:         0
        .size:           8
        .value_kind:     global_buffer
      - .actual_access:  read_only
        .address_space:  global
        .offset:         8
        .size:           8
        .value_kind:     global_buffer
      - .address_space:  global
        .offset:         16
        .size:           8
        .value_kind:     global_buffer
      - .actual_access:  write_only
        .address_space:  global
        .offset:         24
        .size:           8
        .value_kind:     global_buffer
    .group_segment_fixed_size: 46400
    .kernarg_segment_align: 8
    .kernarg_segment_size: 32
    .language:       OpenCL C
    .language_version:
      - 2
      - 0
    .max_flat_workgroup_size: 640
    .name:           _Z6k1_gatPKfS0_PfS1_
    .private_segment_fixed_size: 0
    .sgpr_count:     38
    .sgpr_spill_count: 0
    .symbol:         _Z6k1_gatPKfS0_PfS1_.kd
    .uniform_work_group_size: 1
    .uses_dynamic_stack: false
    .vgpr_count:     124
    .vgpr_spill_count: 0
    .wavefront_size: 64
  - .agpr_count:     0
    .args:
      - .actual_access:  read_only
        .address_space:  global
        .offset:         0
        .size:           8
        .value_kind:     global_buffer
      - .actual_access:  read_only
        .address_space:  global
        .offset:         8
        .size:           8
        .value_kind:     global_buffer
      - .actual_access:  read_only
        .address_space:  global
        .offset:         16
        .size:           8
        .value_kind:     global_buffer
      - .actual_access:  read_only
        .address_space:  global
        .offset:         24
        .size:           8
        .value_kind:     global_buffer
      - .actual_access:  read_only
        .address_space:  global
        .offset:         32
        .size:           8
        .value_kind:     global_buffer
      - .actual_access:  read_only
        .address_space:  global
        .offset:         40
        .size:           8
        .value_kind:     global_buffer
      - .address_space:  global
        .offset:         48
        .size:           8
        .value_kind:     global_buffer
      - .address_space:  global
        .offset:         56
        .size:           8
        .value_kind:     global_buffer
    .group_segment_fixed_size: 64528
    .kernarg_segment_align: 8
    .kernarg_segment_size: 64
    .language:       OpenCL C
    .language_version:
      - 2
      - 0
    .max_flat_workgroup_size: 640
    .name:           _Z7k2_attnPKfS0_S0_S0_S0_S0_PfS1_
    .private_segment_fixed_size: 0
    .sgpr_count:     34
    .sgpr_spill_count: 0
    .symbol:         _Z7k2_attnPKfS0_S0_S0_S0_S0_PfS1_.kd
    .uniform_work_group_size: 1
    .uses_dynamic_stack: false
    .vgpr_count:     102
    .vgpr_spill_count: 0
    .wavefront_size: 64
  - .agpr_count:     0
    .args:
      - .actual_access:  read_only
        .address_space:  global
        .offset:         0
        .size:           8
        .value_kind:     global_buffer
      - .actual_access:  read_only
        .address_space:  global
        .offset:         8
        .size:           8
        .value_kind:     global_buffer
      - .actual_access:  read_only
        .address_space:  global
        .offset:         16
        .size:           8
        .value_kind:     global_buffer
      - .actual_access:  read_only
        .address_space:  global
        .offset:         24
        .size:           8
        .value_kind:     global_buffer
      - .address_space:  global
        .offset:         32
        .size:           8
        .value_kind:     global_buffer
      - .address_space:  global
        .offset:         40
        .size:           8
        .value_kind:     global_buffer
    .group_segment_fixed_size: 97552
    .kernarg_segment_align: 8
    .kernarg_segment_size: 48
    .language:       OpenCL C
    .language_version:
      - 2
      - 0
    .max_flat_workgroup_size: 640
    .name:           _Z5k3_ffPKfS0_S0_S0_PfS1_
    .private_segment_fixed_size: 0
    .sgpr_count:     29
    .sgpr_spill_count: 0
    .symbol:         _Z5k3_ffPKfS0_S0_S0_PfS1_.kd
    .uniform_work_group_size: 1
    .uses_dynamic_stack: false
    .vgpr_count:     88
    .vgpr_spill_count: 0
    .wavefront_size: 64
  - .agpr_count:     0
    .args:
      - .actual_access:  read_only
        .address_space:  global
        .offset:         0
        .size:           8
        .value_kind:     global_buffer
      - .actual_access:  read_only
        .address_space:  global
        .offset:         8
        .size:           8
        .value_kind:     global_buffer
      - .actual_access:  read_only
        .address_space:  global
        .offset:         16
        .size:           8
        .value_kind:     global_buffer
      - .address_space:  global
        .offset:         24
        .size:           8
        .value_kind:     global_buffer
    .group_segment_fixed_size: 8
    .kernarg_segment_align: 8
    .kernarg_segment_size: 32
    .language:       OpenCL C
    .language_version:
      - 2
      - 0
    .max_flat_workgroup_size: 640
    .name:           _Z6k4_ln3PKfS0_S0_Pf
    .private_segment_fixed_size: 0
    .sgpr_count:     21
    .sgpr_spill_count: 0
    .symbol:         _Z6k4_ln3PKfS0_S0_Pf.kd
    .uniform_work_group_size: 1
    .uses_dynamic_stack: false
    .vgpr_count:     50
    .vgpr_spill_count: 0
    .wavefront_size: 64
  - .agpr_count:     0
    .args:
      - .actual_access:  read_only
        .address_space:  global
        .offset:         0
        .size:           8
        .value_kind:     global_buffer
      - .actual_access:  read_only
        .address_space:  global
        .offset:         8
        .size:           8
        .value_kind:     global_buffer
      - .actual_access:  read_only
        .address_space:  global
        .offset:         16
        .size:           8
        .value_kind:     global_buffer
      - .actual_access:  read_only
        .address_space:  global
        .offset:         24
        .size:           8
        .value_kind:     global_buffer
      - .actual_access:  read_only
        .address_space:  global
        .offset:         32
        .size:           8
        .value_kind:     global_buffer
      - .actual_access:  read_only
        .address_space:  global
        .offset:         40
        .size:           8
        .value_kind:     global_buffer
      - .actual_access:  read_only
        .address_space:  global
        .offset:         48
        .size:           8
        .value_kind:     global_buffer
      - .actual_access:  read_only
        .address_space:  global
        .offset:         56
        .size:           8
        .value_kind:     global_buffer
      - .actual_access:  read_only
        .address_space:  global
        .offset:         64
        .size:           8
        .value_kind:     global_buffer
      - .actual_access:  read_only
        .address_space:  global
        .offset:         72
        .size:           8
        .value_kind:     global_buffer
      - .actual_access:  read_only
        .address_space:  global
        .offset:         80
        .size:           8
        .value_kind:     global_buffer
      - .actual_access:  read_only
        .address_space:  global
        .offset:         88
        .size:           8
        .value_kind:     global_buffer
      - .actual_access:  read_only
        .address_space:  global
        .offset:         96
        .size:           8
        .value_kind:     global_buffer
      - .actual_access:  read_only
        .address_space:  global
        .offset:         104
        .size:           8
        .value_kind:     global_buffer
      - .address_space:  global
        .offset:         112
        .size:           8
        .value_kind:     global_buffer
      - .actual_access:  write_only
        .address_space:  global
        .offset:         120
        .size:           8
        .value_kind:     global_buffer
    .group_segment_fixed_size: 147104
    .kernarg_segment_align: 8
    .kernarg_segment_size: 128
    .language:       OpenCL C
    .language_version:
      - 2
      - 0
    .max_flat_workgroup_size: 640
    .name:           _Z7k_fusedPKfS0_S0_S0_S0_S0_S0_S0_S0_S0_S0_S0_S0_S0_PfS1_
    .private_segment_fixed_size: 0
    .sgpr_count:     62
    .sgpr_spill_count: 0
    .symbol:         _Z7k_fusedPKfS0_S0_S0_S0_S0_S0_S0_S0_S0_S0_S0_S0_S0_PfS1_.kd
    .uniform_work_group_size: 1
    .uses_dynamic_stack: false
    .vgpr_count:     168
    .vgpr_spill_count: 0
    .wavefront_size: 64
